# mixer-output int8 quantisation: next token row requested one iteration ahead (on top of v10)
# speedup vs baseline: 1.0330x; 1.0019x over previous
.LBB0_1524:
	s_or_b64 exec, exec, s[8:9]
	s_mov_b64 s[8:9], s[0:1]
	s_mov_b64 s[12:13], s[0:1]
	s_mov_b64 s[14:15], s[0:1]
	v_mov_b32_e32 v3, v0
	s_waitcnt lgkmcnt(0)
	s_barrier
	s_movk_i32 s3, 0x2000
	v_ashrrev_i32_e32 v2, 6, v3
	v_add_u32_e32 v2, s84, v2
	v_cmp_gt_i32_e32 vcc, s3, v2
	s_and_saveexec_b64 s[10:11], vcc
	s_cbranch_execz .LBB0_1529
	s_load_dwordx2 s[16:17], s[14:15], 0x90
	s_load_dwordx2 s[18:19], s[8:9], 0x90
	s_load_dwordx2 s[20:21], s[12:13], 0x90
	v_and_b32_e32 v3, 63, v3
	v_lshlrev_b32_e32 v6, 4, v3
	v_mov_b32_e32 v7, 0
	s_waitcnt lgkmcnt(0)
	v_lshl_add_u64 v[4:5], s[18:19], 0, v[6:7]
	s_mov_b64 s[8:9], 0x34400000
	v_lshlrev_b32_e32 v6, 3, v3
	v_lshl_add_u64 v[4:5], v[4:5], 0, s[8:9]
	v_lshl_add_u64 v[6:7], s[20:21], 0, v[6:7]
	s_mov_b64 s[8:9], 0x1e400000
	v_cmp_lt_i32_e32 vcc, v157, v154
	v_lshl_add_u64 v[6:7], v[6:7], 0, s[8:9]
	v_cmp_eq_u32_e64 s[8:9], 0, v3
	v_cndmask_b32_e32 v3, v1, v157, vcc
	v_cmp_lt_i32_e32 vcc, v158, v154
	v_lshlrev_b32_e32 v10, 2, v3
	s_add_u32 s12, s16, 0x20400000
	v_cndmask_b32_e32 v3, v1, v158, vcc
	v_cmp_lt_i32_e32 vcc, v159, v154
	v_lshlrev_b32_e32 v11, 2, v3
	s_addc_u32 s13, s17, 0
	v_cndmask_b32_e32 v3, v1, v159, vcc
	v_cmp_lt_i32_e32 vcc, v160, v154
	v_lshlrev_b32_e32 v12, 2, v3
	s_lshl_b32 s3, s46, 3
	v_cndmask_b32_e32 v3, v1, v160, vcc
	v_cmp_lt_i32_e32 vcc, v156, v154
	v_lshlrev_b32_e32 v13, 2, v3
	s_mov_b64 s[14:15], 0
	v_cndmask_b32_e32 v3, v1, v156, vcc
	v_cmp_lt_i32_e32 vcc, v155, v154
	v_lshlrev_b32_e32 v14, 2, v3
	s_movk_i32 s18, 0x1000
	v_cndmask_b32_e32 v3, v1, v155, vcc
	v_lshlrev_b32_e32 v15, 2, v3
	s_mov_b32 s19, 0xda24260
	s_mov_b32 s20, 0xc0c0500
	s_movk_i32 s21, 0x1fff
	s_mov_b64 s[98:99], 0x1000
	v_ashrrev_i32_e32 v3, 31, v2
	v_lshlrev_b64 v[8:9], 13, v[2:3]
	v_lshl_add_u64 v[196:197], v[4:5], 0, v[8:9]
	v_lshl_add_u64 v[198:199], v[196:197], 0, s[98:99]
	global_load_dwordx4 v[164:167], v[196:197], off
	global_load_dwordx4 v[168:171], v[196:197], off offset:1024
	global_load_dwordx4 v[172:175], v[196:197], off offset:2048
	global_load_dwordx4 v[176:179], v[196:197], off offset:3072
	global_load_dwordx4 v[180:183], v[198:199], off
	global_load_dwordx4 v[184:187], v[198:199], off offset:1024
	global_load_dwordx4 v[188:191], v[198:199], off offset:2048
	global_load_dwordx4 v[192:195], v[198:199], off offset:3072
	s_waitcnt vmcnt(0)
	s_branch .LBB0_1527

.LBB0_1527:
	v_ashrrev_i32_e32 v3, 31, v2
	v_lshlrev_b64 v[8:9], 13, v[2:3]
	v_lshl_add_u64 v[8:9], v[4:5], 0, v[8:9]
	s_waitcnt vmcnt(8)
	v_mov_b32_e32 v16, v164
	v_mov_b32_e32 v17, v165
	v_mov_b32_e32 v18, v166
	v_mov_b32_e32 v19, v167
	v_mov_b32_e32 v20, v168
	v_mov_b32_e32 v21, v169
	v_mov_b32_e32 v22, v170
	v_mov_b32_e32 v23, v171
	v_mov_b32_e32 v24, v172
	v_mov_b32_e32 v25, v173
	v_mov_b32_e32 v26, v174
	v_mov_b32_e32 v27, v175
	v_mov_b32_e32 v28, v176
	v_mov_b32_e32 v29, v177
	v_mov_b32_e32 v30, v178
	v_mov_b32_e32 v31, v179
	v_mov_b32_e32 v32, v180
	v_mov_b32_e32 v33, v181
	v_mov_b32_e32 v34, v182
	v_mov_b32_e32 v35, v183
	v_mov_b32_e32 v36, v184
	v_mov_b32_e32 v37, v185
	v_mov_b32_e32 v38, v186
	v_mov_b32_e32 v39, v187
	v_mov_b32_e32 v40, v188
	v_mov_b32_e32 v41, v189
	v_mov_b32_e32 v42, v190
	v_mov_b32_e32 v43, v191
	v_mov_b32_e32 v44, v192
	v_mov_b32_e32 v45, v193
	v_mov_b32_e32 v46, v194
	v_mov_b32_e32 v47, v195
	v_add_u32_e32 v200, s3, v2
	v_min_i32_e32 v200, 0x1fff, v200
	v_ashrrev_i32_e32 v201, 31, v200
	v_lshlrev_b64 v[200:201], 13, v[200:201]
	v_lshl_add_u64 v[196:197], v[4:5], 0, v[200:201]
	v_lshl_add_u64 v[198:199], v[196:197], 0, s[98:99]
	global_load_dwordx4 v[164:167], v[196:197], off
	global_load_dwordx4 v[168:171], v[196:197], off offset:1024
	global_load_dwordx4 v[172:175], v[196:197], off offset:2048
	global_load_dwordx4 v[176:179], v[196:197], off offset:3072
	global_load_dwordx4 v[180:183], v[198:199], off
	global_load_dwordx4 v[184:187], v[198:199], off offset:1024
	global_load_dwordx4 v[188:191], v[198:199], off offset:2048
	global_load_dwordx4 v[192:195], v[198:199], off offset:3072
	v_add_co_u32_e32 v8, vcc, s18, v8
	s_nop 0
	v_lshlrev_b32_e32 v48, 16, v16
	v_addc_co_u32_e32 v9, vcc, 0, v9, vcc
	v_and_b32_e32 v49, 0xffff0000, v16
	v_lshlrev_b32_e32 v50, 16, v17
	v_and_b32_e32 v17, 0xffff0000, v17
	v_lshlrev_b32_e32 v51, 16, v18
	v_and_b32_e32 v52, 0xffff0000, v18
	v_lshlrev_b32_e32 v53, 16, v19
	v_and_b32_e32 v19, 0xffff0000, v19
	v_max_f32_e64 v8, |v49|, |v49|
	v_max_f32_e64 v9, |v48|, |v48|
	v_max_f32_e64 v16, |v17|, |v17|
	v_max_f32_e64 v18, |v50|, |v50|
	s_nop 0
	v_lshlrev_b32_e32 v54, 16, v20
	v_and_b32_e32 v20, 0xffff0000, v20
	v_lshlrev_b32_e32 v55, 16, v21
	v_and_b32_e32 v21, 0xffff0000, v21
	v_max_f32_e64 v65, |v52|, |v52|
	v_max_f32_e64 v66, |v51|, |v51|
	v_max_f32_e64 v67, |v19|, |v19|
	v_max_f32_e64 v68, |v53|, |v53|
	v_max_f32_e32 v8, v9, v8
	v_max_f32_e32 v9, v18, v16
	v_lshlrev_b32_e32 v56, 16, v22
	v_and_b32_e32 v22, 0xffff0000, v22
	v_lshlrev_b32_e32 v57, 16, v23
	v_and_b32_e32 v23, 0xffff0000, v23
	v_max_f32_e64 v69, |v20|, |v20|
	v_max_f32_e64 v70, |v54|, |v54|
	v_max_f32_e64 v71, |v21|, |v21|
	v_max_f32_e64 v72, |v55|, |v55|
	v_max_f32_e32 v16, v66, v65
	v_max_f32_e32 v18, v68, v67
	v_max3_f32 v8, v8, 0, v9
	s_nop 0
	v_lshlrev_b32_e32 v58, 16, v24
	v_and_b32_e32 v24, 0xffff0000, v24
	v_lshlrev_b32_e32 v59, 16, v25
	v_and_b32_e32 v25, 0xffff0000, v25
	v_max_f32_e64 v73, |v22|, |v22|
	v_max_f32_e64 v74, |v56|, |v56|
	v_max_f32_e64 v75, |v23|, |v23|
	v_max_f32_e64 v76, |v57|, |v57|
	v_max_f32_e32 v65, v70, v69
	v_max_f32_e32 v66, v72, v71
	v_max3_f32 v8, v8, v16, v18
	v_lshlrev_b32_e32 v60, 16, v26
	v_and_b32_e32 v26, 0xffff0000, v26
	v_lshlrev_b32_e32 v61, 16, v27
	v_and_b32_e32 v27, 0xffff0000, v27
	v_max_f32_e64 v77, |v24|, |v24|
	v_max_f32_e64 v78, |v58|, |v58|
	v_max_f32_e64 v79, |v25|, |v25|
	v_max_f32_e64 v80, |v59|, |v59|
	v_max_f32_e32 v67, v74, v73
	v_max_f32_e32 v68, v76, v75
	v_max3_f32 v8, v8, v65, v66
	s_nop 0
	v_lshlrev_b32_e32 v62, 16, v28
	v_and_b32_e32 v28, 0xffff0000, v28
	v_lshlrev_b32_e32 v63, 16, v29
	v_and_b32_e32 v29, 0xffff0000, v29
	v_lshlrev_b32_e32 v64, 16, v30
	v_max_f32_e64 v81, |v26|, |v26|
	v_max_f32_e64 v82, |v60|, |v60|
	v_max_f32_e64 v83, |v27|, |v27|
	v_max_f32_e64 v84, |v61|, |v61|
	v_max_f32_e32 v69, v78, v77
	v_max_f32_e32 v70, v80, v79
	v_max3_f32 v8, v8, v67, v68
	v_and_b32_e32 v30, 0xffff0000, v30
	v_max_f32_e64 v85, |v28|, |v28|
	v_max_f32_e64 v86, |v62|, |v62|
	v_max_f32_e64 v87, |v29|, |v29|
	v_max_f32_e64 v88, |v63|, |v63|
	v_max_f32_e32 v71, v82, v81
	v_max_f32_e32 v72, v84, v83
	v_max3_f32 v8, v8, v69, v70
	v_max_f32_e64 v9, |v30|, |v30|
	v_max_f32_e64 v16, |v64|, |v64|
	v_lshlrev_b32_e32 v65, 16, v31
	v_and_b32_e32 v31, 0xffff0000, v31
	v_max_f32_e32 v73, v86, v85
	v_max_f32_e32 v74, v88, v87
	v_max3_f32 v8, v8, v71, v72
	v_max_f32_e32 v9, v16, v9
	v_max_f32_e64 v16, |v31|, |v31|
	v_max_f32_e64 v18, |v65|, |v65|
	v_max3_f32 v8, v8, v73, v74
	v_max_f32_e32 v16, v18, v16
	s_nop 0
	v_lshlrev_b32_e32 v66, 16, v32
	v_and_b32_e32 v32, 0xffff0000, v32
	v_max3_f32 v8, v8, v9, v16
	v_max_f32_e64 v9, |v32|, |v32|
	v_max_f32_e64 v16, |v66|, |v66|
	v_lshlrev_b32_e32 v67, 16, v33
	v_and_b32_e32 v33, 0xffff0000, v33
	v_max_f32_e32 v9, v16, v9
	v_max_f32_e64 v16, |v33|, |v33|
	v_max_f32_e64 v18, |v67|, |v67|
	v_max_f32_e32 v16, v18, v16
	v_lshlrev_b32_e32 v68, 16, v34
	v_and_b32_e32 v34, 0xffff0000, v34
	v_max3_f32 v8, v8, v9, v16
	v_max_f32_e64 v9, |v34|, |v34|
	v_max_f32_e64 v16, |v68|, |v68|
	v_lshlrev_b32_e32 v69, 16, v35
	v_and_b32_e32 v35, 0xffff0000, v35
	v_max_f32_e32 v9, v16, v9
	v_max_f32_e64 v16, |v35|, |v35|
	v_max_f32_e64 v18, |v69|, |v69|
	v_max_f32_e32 v16, v18, v16
	s_nop 0
	v_lshlrev_b32_e32 v70, 16, v36
	v_and_b32_e32 v36, 0xffff0000, v36
	v_max3_f32 v8, v8, v9, v16
	v_max_f32_e64 v9, |v36|, |v36|
	v_max_f32_e64 v16, |v70|, |v70|
	v_lshlrev_b32_e32 v71, 16, v37
	v_and_b32_e32 v37, 0xffff0000, v37
	v_max_f32_e32 v9, v16, v9
	v_max_f32_e64 v16, |v37|, |v37|
	v_max_f32_e64 v18, |v71|, |v71|
	v_max_f32_e32 v16, v18, v16
	v_lshlrev_b32_e32 v72, 16, v38
	v_and_b32_e32 v38, 0xffff0000, v38
	v_max3_f32 v8, v8, v9, v16
	v_max_f32_e64 v9, |v38|, |v38|
	v_max_f32_e64 v16, |v72|, |v72|
	v_lshlrev_b32_e32 v73, 16, v39
	v_and_b32_e32 v39, 0xffff0000, v39
	v_max_f32_e32 v9, v16, v9
	v_max_f32_e64 v16, |v39|, |v39|
	v_max_f32_e64 v18, |v73|, |v73|
	v_max_f32_e32 v16, v18, v16
	s_nop 0
	v_lshlrev_b32_e32 v74, 16, v40
	v_and_b32_e32 v40, 0xffff0000, v40
	v_max3_f32 v8, v8, v9, v16
	v_max_f32_e64 v9, |v40|, |v40|
	v_max_f32_e64 v16, |v74|, |v74|
	v_lshlrev_b32_e32 v75, 16, v41
	v_and_b32_e32 v41, 0xffff0000, v41
	v_max_f32_e32 v9, v16, v9
	v_max_f32_e64 v16, |v41|, |v41|
	v_max_f32_e64 v18, |v75|, |v75|
	v_max_f32_e32 v16, v18, v16
	v_lshlrev_b32_e32 v76, 16, v42
	v_and_b32_e32 v42, 0xffff0000, v42
	v_max3_f32 v8, v8, v9, v16
	v_max_f32_e64 v9, |v42|, |v42|
	v_max_f32_e64 v16, |v76|, |v76|
	v_lshlrev_b32_e32 v77, 16, v43
	v_and_b32_e32 v43, 0xffff0000, v43
	v_max_f32_e32 v9, v16, v9
	v_max_f32_e64 v16, |v43|, |v43|
	v_max_f32_e64 v18, |v77|, |v77|
	v_max_f32_e32 v16, v18, v16
	s_nop 0
	v_lshlrev_b32_e32 v78, 16, v44
	v_and_b32_e32 v44, 0xffff0000, v44
	v_max3_f32 v8, v8, v9, v16
	v_max_f32_e64 v9, |v44|, |v44|
	v_max_f32_e64 v16, |v78|, |v78|
	v_lshlrev_b32_e32 v79, 16, v45
	v_and_b32_e32 v45, 0xffff0000, v45
	v_max_f32_e32 v9, v16, v9
	v_max_f32_e64 v16, |v45|, |v45|
	v_max_f32_e64 v18, |v79|, |v79|
	v_max_f32_e32 v16, v18, v16
	v_lshlrev_b32_e32 v80, 16, v46
	v_and_b32_e32 v46, 0xffff0000, v46
	v_max3_f32 v8, v8, v9, v16
	v_max_f32_e64 v9, |v46|, |v46|
	v_max_f32_e64 v16, |v80|, |v80|
	v_lshlrev_b32_e32 v81, 16, v47
	v_and_b32_e32 v47, 0xffff0000, v47
	v_max_f32_e32 v9, v16, v9
	v_max_f32_e64 v16, |v47|, |v47|
	v_max_f32_e64 v18, |v81|, |v81|
	v_max_f32_e32 v16, v18, v16
	v_max3_f32 v8, v8, v9, v16
	ds_bpermute_b32 v9, v10, v8
	s_waitcnt lgkmcnt(0)
	v_max_f32_e32 v9, v9, v9
	v_max_f32_e32 v8, v8, v9
	ds_bpermute_b32 v9, v11, v8
	s_waitcnt lgkmcnt(0)
	v_max_f32_e32 v9, v9, v9
	v_max_f32_e32 v8, v8, v9
	ds_bpermute_b32 v9, v12, v8
	s_waitcnt lgkmcnt(0)
	v_max_f32_e32 v9, v9, v9
	v_max_f32_e32 v8, v8, v9
	ds_bpermute_b32 v9, v13, v8
	s_waitcnt lgkmcnt(0)
	v_max_f32_e32 v9, v9, v9
	v_max_f32_e32 v8, v8, v9
	ds_bpermute_b32 v9, v14, v8
	s_waitcnt lgkmcnt(0)
	v_max_f32_e32 v9, v9, v9
	v_max_f32_e32 v8, v8, v9
	ds_bpermute_b32 v9, v15, v8
	s_waitcnt lgkmcnt(0)
	v_max3_f32 v8, v8, v9, s19
	v_mul_f32_e32 v16, 0x3c010204, v8
	v_div_scale_f32 v18, s[16:17], v16, v16, 1.0
	v_rcp_f32_e32 v82, v18
	v_lshlrev_b64 v[8:9], 12, v[2:3]
	v_lshl_add_u64 v[8:9], v[6:7], 0, v[8:9]
	v_fma_f32 v83, -v18, v82, 1.0
	v_fmac_f32_e32 v82, v83, v82
	v_div_scale_f32 v83, vcc, 1.0, v16, 1.0
	v_mul_f32_e32 v84, v83, v82
	v_fma_f32 v85, -v18, v84, v83
	v_fmac_f32_e32 v84, v85, v82
	v_fma_f32 v18, -v18, v84, v83
	v_div_fmas_f32 v18, v18, v82, v84
	v_div_fixup_f32 v82, v18, v16, 1.0
	v_mul_f32_e32 v18, v82, v48
	v_mul_f32_e32 v48, v82, v49
	v_rndne_f32_e32 v48, v48
	v_mul_f32_e32 v49, v82, v50
	v_rndne_f32_e32 v18, v18
	v_cvt_i32_f32_e32 v48, v48
	v_rndne_f32_e32 v49, v49
	v_mul_f32_e32 v17, v82, v17
	v_cvt_i32_f32_e32 v18, v18
	v_cvt_i32_f32_sdwa v49, v49 dst_sel:WORD_1 dst_unused:UNUSED_PAD src0_sel:DWORD
	v_rndne_f32_e32 v17, v17
	v_cvt_i32_f32_sdwa v17, v17 dst_sel:BYTE_3 dst_unused:UNUSED_PAD src0_sel:DWORD
	v_lshlrev_b32_e32 v48, 8, v48
	v_and_b32_e32 v49, 0xff0000, v49
	v_perm_b32 v18, v48, v18, s20
	v_mul_f32_e32 v48, v82, v52
	v_or3_b32 v18, v18, v17, v49
	v_mul_f32_e32 v17, v82, v51
	v_rndne_f32_e32 v48, v48
	v_mul_f32_e32 v49, v82, v53
	v_rndne_f32_e32 v17, v17
	v_cvt_i32_f32_e32 v48, v48
	v_rndne_f32_e32 v49, v49
	v_mul_f32_e32 v19, v82, v19
	v_cvt_i32_f32_e32 v17, v17
	v_cvt_i32_f32_sdwa v49, v49 dst_sel:WORD_1 dst_unused:UNUSED_PAD src0_sel:DWORD
	v_rndne_f32_e32 v19, v19
	v_cvt_i32_f32_sdwa v19, v19 dst_sel:BYTE_3 dst_unused:UNUSED_PAD src0_sel:DWORD
	v_lshlrev_b32_e32 v48, 8, v48
	v_and_b32_e32 v49, 0xff0000, v49
	v_perm_b32 v17, v48, v17, s20
	v_or3_b32 v19, v17, v19, v49
	global_store_dwordx2 v[8:9], v[18:19], off
	v_mul_f32_e32 v18, v82, v20
	v_mul_f32_e32 v17, v82, v54
	v_rndne_f32_e32 v18, v18
	v_mul_f32_e32 v19, v82, v55
	v_rndne_f32_e32 v17, v17
	v_cvt_i32_f32_e32 v18, v18
	v_rndne_f32_e32 v19, v19
	v_mul_f32_e32 v20, v82, v21
	v_cvt_i32_f32_e32 v17, v17
	v_cvt_i32_f32_sdwa v19, v19 dst_sel:WORD_1 dst_unused:UNUSED_PAD src0_sel:DWORD
	v_rndne_f32_e32 v20, v20
	v_cvt_i32_f32_sdwa v20, v20 dst_sel:BYTE_3 dst_unused:UNUSED_PAD src0_sel:DWORD
	v_lshlrev_b32_e32 v18, 8, v18
	v_and_b32_e32 v19, 0xff0000, v19
	v_perm_b32 v17, v18, v17, s20
	v_or3_b32 v18, v17, v20, v19
	v_mul_f32_e32 v19, v82, v22
	v_mul_f32_e32 v17, v82, v56
	v_rndne_f32_e32 v19, v19
	v_mul_f32_e32 v20, v82, v57
	v_rndne_f32_e32 v17, v17
	v_cvt_i32_f32_e32 v19, v19
	v_rndne_f32_e32 v20, v20
	v_mul_f32_e32 v21, v82, v23
	v_cvt_i32_f32_e32 v17, v17
	v_cvt_i32_f32_sdwa v20, v20 dst_sel:WORD_1 dst_unused:UNUSED_PAD src0_sel:DWORD
	v_rndne_f32_e32 v21, v21
	v_cvt_i32_f32_sdwa v21, v21 dst_sel:BYTE_3 dst_unused:UNUSED_PAD src0_sel:DWORD
	v_lshlrev_b32_e32 v19, 8, v19
	v_and_b32_e32 v20, 0xff0000, v20
	v_perm_b32 v17, v19, v17, s20
	v_or3_b32 v19, v17, v21, v20
	global_store_dwordx2 v[8:9], v[18:19], off offset:512
	v_mul_f32_e32 v18, v82, v24
	v_mul_f32_e32 v17, v82, v58
	v_rndne_f32_e32 v18, v18
	v_mul_f32_e32 v19, v82, v59
	v_rndne_f32_e32 v17, v17
	v_cvt_i32_f32_e32 v18, v18
	v_rndne_f32_e32 v19, v19
	v_mul_f32_e32 v20, v82, v25
	v_cvt_i32_f32_e32 v17, v17
	v_cvt_i32_f32_sdwa v19, v19 dst_sel:WORD_1 dst_unused:UNUSED_PAD src0_sel:DWORD
	v_rndne_f32_e32 v20, v20
	v_cvt_i32_f32_sdwa v20, v20 dst_sel:BYTE_3 dst_unused:UNUSED_PAD src0_sel:DWORD
	v_lshlrev_b32_e32 v18, 8, v18
	v_and_b32_e32 v19, 0xff0000, v19
	v_perm_b32 v17, v18, v17, s20
	v_or3_b32 v18, v17, v20, v19
	v_mul_f32_e32 v19, v82, v26
	v_mul_f32_e32 v17, v82, v60
	v_rndne_f32_e32 v19, v19
	v_mul_f32_e32 v20, v82, v61
	v_rndne_f32_e32 v17, v17
	v_cvt_i32_f32_e32 v19, v19
	v_rndne_f32_e32 v20, v20
	v_mul_f32_e32 v21, v82, v27
	v_cvt_i32_f32_e32 v17, v17
	v_cvt_i32_f32_sdwa v20, v20 dst_sel:WORD_1 dst_unused:UNUSED_PAD src0_sel:DWORD
	v_rndne_f32_e32 v21, v21
	v_cvt_i32_f32_sdwa v21, v21 dst_sel:BYTE_3 dst_unused:UNUSED_PAD src0_sel:DWORD
	v_lshlrev_b32_e32 v19, 8, v19
	v_and_b32_e32 v20, 0xff0000, v20
	v_perm_b32 v17, v19, v17, s20
	v_or3_b32 v19, v17, v21, v20
	global_store_dwordx2 v[8:9], v[18:19], off offset:1024
	v_mul_f32_e32 v18, v82, v28
	v_mul_f32_e32 v17, v82, v62
	v_rndne_f32_e32 v18, v18
	v_mul_f32_e32 v19, v82, v63
	v_rndne_f32_e32 v17, v17
	v_cvt_i32_f32_e32 v18, v18
	v_rndne_f32_e32 v19, v19
	v_mul_f32_e32 v20, v82, v29
	v_cvt_i32_f32_e32 v17, v17
	v_cvt_i32_f32_sdwa v19, v19 dst_sel:WORD_1 dst_unused:UNUSED_PAD src0_sel:DWORD
	v_rndne_f32_e32 v20, v20
	v_cvt_i32_f32_sdwa v20, v20 dst_sel:BYTE_3 dst_unused:UNUSED_PAD src0_sel:DWORD
	v_lshlrev_b32_e32 v18, 8, v18
	v_and_b32_e32 v19, 0xff0000, v19
	v_perm_b32 v17, v18, v17, s20
	v_or3_b32 v18, v17, v20, v19
	v_mul_f32_e32 v19, v82, v30
	v_mul_f32_e32 v17, v82, v64
	v_rndne_f32_e32 v19, v19
	v_mul_f32_e32 v20, v82, v65
	v_rndne_f32_e32 v17, v17
	v_cvt_i32_f32_e32 v19, v19
	v_rndne_f32_e32 v20, v20
	v_mul_f32_e32 v21, v82, v31
	v_cvt_i32_f32_e32 v17, v17
	v_cvt_i32_f32_sdwa v20, v20 dst_sel:WORD_1 dst_unused:UNUSED_PAD src0_sel:DWORD
	v_rndne_f32_e32 v21, v21
	v_cvt_i32_f32_sdwa v21, v21 dst_sel:BYTE_3 dst_unused:UNUSED_PAD src0_sel:DWORD
	v_lshlrev_b32_e32 v19, 8, v19
	v_and_b32_e32 v20, 0xff0000, v20
	v_perm_b32 v17, v19, v17, s20
	v_or3_b32 v19, v17, v21, v20
	global_store_dwordx2 v[8:9], v[18:19], off offset:1536
	v_mul_f32_e32 v18, v82, v32
	v_mul_f32_e32 v17, v82, v66
	v_rndne_f32_e32 v18, v18
	v_mul_f32_e32 v19, v82, v67
	v_rndne_f32_e32 v17, v17
	v_cvt_i32_f32_e32 v18, v18
	v_rndne_f32_e32 v19, v19
	v_mul_f32_e32 v20, v82, v33
	v_cvt_i32_f32_e32 v17, v17
	v_cvt_i32_f32_sdwa v19, v19 dst_sel:WORD_1 dst_unused:UNUSED_PAD src0_sel:DWORD
	v_rndne_f32_e32 v20, v20
	v_cvt_i32_f32_sdwa v20, v20 dst_sel:BYTE_3 dst_unused:UNUSED_PAD src0_sel:DWORD
	v_lshlrev_b32_e32 v18, 8, v18
	v_and_b32_e32 v19, 0xff0000, v19
	v_perm_b32 v17, v18, v17, s20
	v_or3_b32 v18, v17, v20, v19
	v_mul_f32_e32 v19, v82, v34
	v_mul_f32_e32 v17, v82, v68
	v_rndne_f32_e32 v19, v19
	v_mul_f32_e32 v20, v82, v69
	v_rndne_f32_e32 v17, v17
	v_cvt_i32_f32_e32 v19, v19
	v_rndne_f32_e32 v20, v20
	v_mul_f32_e32 v21, v82, v35
	v_cvt_i32_f32_e32 v17, v17
	v_cvt_i32_f32_sdwa v20, v20 dst_sel:WORD_1 dst_unused:UNUSED_PAD src0_sel:DWORD
	v_rndne_f32_e32 v21, v21
	v_cvt_i32_f32_sdwa v21, v21 dst_sel:BYTE_3 dst_unused:UNUSED_PAD src0_sel:DWORD
	v_lshlrev_b32_e32 v19, 8, v19
	v_and_b32_e32 v20, 0xff0000, v20
	v_perm_b32 v17, v19, v17, s20
	v_or3_b32 v19, v17, v21, v20
	global_store_dwordx2 v[8:9], v[18:19], off offset:2048
	v_mul_f32_e32 v18, v82, v36
	v_mul_f32_e32 v17, v82, v70
	v_rndne_f32_e32 v18, v18
	v_mul_f32_e32 v19, v82, v71
	v_rndne_f32_e32 v17, v17
	v_cvt_i32_f32_e32 v18, v18
	v_rndne_f32_e32 v19, v19
	v_mul_f32_e32 v20, v82, v37
	v_cvt_i32_f32_e32 v17, v17
	v_cvt_i32_f32_sdwa v19, v19 dst_sel:WORD_1 dst_unused:UNUSED_PAD src0_sel:DWORD
	v_rndne_f32_e32 v20, v20
	v_cvt_i32_f32_sdwa v20, v20 dst_sel:BYTE_3 dst_unused:UNUSED_PAD src0_sel:DWORD
	v_lshlrev_b32_e32 v18, 8, v18
	v_and_b32_e32 v19, 0xff0000, v19
	v_perm_b32 v17, v18, v17, s20
	v_or3_b32 v18, v17, v20, v19
	v_mul_f32_e32 v19, v82, v38
	v_mul_f32_e32 v17, v82, v72
	v_rndne_f32_e32 v19, v19
	v_mul_f32_e32 v20, v82, v73
	v_rndne_f32_e32 v17, v17
	v_cvt_i32_f32_e32 v19, v19
	v_rndne_f32_e32 v20, v20
	v_mul_f32_e32 v21, v82, v39
	v_cvt_i32_f32_e32 v17, v17
	v_cvt_i32_f32_sdwa v20, v20 dst_sel:WORD_1 dst_unused:UNUSED_PAD src0_sel:DWORD
	v_rndne_f32_e32 v21, v21
	v_cvt_i32_f32_sdwa v21, v21 dst_sel:BYTE_3 dst_unused:UNUSED_PAD src0_sel:DWORD
	v_lshlrev_b32_e32 v19, 8, v19
	v_and_b32_e32 v20, 0xff0000, v20
	v_perm_b32 v17, v19, v17, s20
	v_or3_b32 v19, v17, v21, v20
	global_store_dwordx2 v[8:9], v[18:19], off offset:2560
	v_mul_f32_e32 v18, v82, v40
	v_mul_f32_e32 v17, v82, v74
	v_rndne_f32_e32 v18, v18
	v_mul_f32_e32 v19, v82, v75
	v_rndne_f32_e32 v17, v17
	v_cvt_i32_f32_e32 v18, v18
	v_rndne_f32_e32 v19, v19
	v_mul_f32_e32 v20, v82, v41
	v_cvt_i32_f32_e32 v17, v17
	v_cvt_i32_f32_sdwa v19, v19 dst_sel:WORD_1 dst_unused:UNUSED_PAD src0_sel:DWORD
	v_rndne_f32_e32 v20, v20
	v_cvt_i32_f32_sdwa v20, v20 dst_sel:BYTE_3 dst_unused:UNUSED_PAD src0_sel:DWORD
	v_lshlrev_b32_e32 v18, 8, v18
	v_and_b32_e32 v19, 0xff0000, v19
	v_perm_b32 v17, v18, v17, s20
	v_or3_b32 v18, v17, v20, v19
	v_mul_f32_e32 v19, v82, v42
	v_mul_f32_e32 v17, v82, v76
	v_rndne_f32_e32 v19, v19
	v_mul_f32_e32 v20, v82, v77
	v_rndne_f32_e32 v17, v17
	v_cvt_i32_f32_e32 v19, v19
	v_rndne_f32_e32 v20, v20
	v_mul_f32_e32 v21, v82, v43
	v_cvt_i32_f32_e32 v17, v17
	v_cvt_i32_f32_sdwa v20, v20 dst_sel:WORD_1 dst_unused:UNUSED_PAD src0_sel:DWORD
	v_rndne_f32_e32 v21, v21
	v_cvt_i32_f32_sdwa v21, v21 dst_sel:BYTE_3 dst_unused:UNUSED_PAD src0_sel:DWORD
	v_lshlrev_b32_e32 v19, 8, v19
	v_and_b32_e32 v20, 0xff0000, v20
	v_perm_b32 v17, v19, v17, s20
	v_or3_b32 v19, v17, v21, v20
	global_store_dwordx2 v[8:9], v[18:19], off offset:3072
	v_mul_f32_e32 v18, v82, v44
	v_mul_f32_e32 v17, v82, v78
	v_rndne_f32_e32 v18, v18
	v_mul_f32_e32 v19, v82, v79
	v_rndne_f32_e32 v17, v17
	v_cvt_i32_f32_e32 v18, v18
	v_rndne_f32_e32 v19, v19
	v_mul_f32_e32 v20, v82, v45
	v_cvt_i32_f32_e32 v17, v17
	v_cvt_i32_f32_sdwa v19, v19 dst_sel:WORD_1 dst_unused:UNUSED_PAD src0_sel:DWORD
	v_rndne_f32_e32 v20, v20
	v_cvt_i32_f32_sdwa v20, v20 dst_sel:BYTE_3 dst_unused:UNUSED_PAD src0_sel:DWORD
	v_lshlrev_b32_e32 v18, 8, v18
	v_and_b32_e32 v19, 0xff0000, v19
	v_perm_b32 v17, v18, v17, s20
	v_or3_b32 v18, v17, v20, v19
	v_mul_f32_e32 v19, v82, v46
	v_mul_f32_e32 v17, v82, v80
	v_rndne_f32_e32 v19, v19
	v_mul_f32_e32 v20, v82, v81
	v_rndne_f32_e32 v17, v17
	v_cvt_i32_f32_e32 v19, v19
	v_rndne_f32_e32 v20, v20
	v_mul_f32_e32 v21, v82, v47
	v_cvt_i32_f32_e32 v17, v17
	v_cvt_i32_f32_sdwa v20, v20 dst_sel:WORD_1 dst_unused:UNUSED_PAD src0_sel:DWORD
	v_rndne_f32_e32 v21, v21
	v_cvt_i32_f32_sdwa v21, v21 dst_sel:BYTE_3 dst_unused:UNUSED_PAD src0_sel:DWORD
	v_lshlrev_b32_e32 v19, 8, v19
	v_and_b32_e32 v20, 0xff0000, v20
	v_perm_b32 v17, v19, v17, s20
	v_or3_b32 v19, v17, v21, v20
	global_store_dwordx2 v[8:9], v[18:19], off offset:3584
	s_and_saveexec_b64 s[16:17], s[8:9]
	s_cbranch_execz .LBB0_1526
	v_lshl_add_u64 v[8:9], v[2:3], 2, s[12:13]
	global_store_dword v[8:9], v16, off
	s_branch .LBB0_1526
